# DSA selection-mask rebuild: rows loaded in two groups of four (was eight serial load-wait trips)
# speedup vs baseline: 1.0149x; 1.0016x over previous
.LBB0_1636:
	s_mov_b64 s[36:37], vcc
	s_and_saveexec_b64 s[10:11], vcc
	v_ashrrev_i32_e32 v90, 8, v20
	v_lshlrev_b32_e32 v90, 10, v90
	v_mov_b32_e32 v91, v3
	v_lshl_add_u64 v[90:91], v[4:5], 0, v[90:91]
	v_add_co_u32_e32 v98, vcc, 0x1000, v90
	s_nop 1
	v_addc_co_u32_e32 v99, vcc, 0, v91, vcc
	global_load_dwordx4 v[100:103], v[90:91], off
	global_load_dwordx4 v[104:107], v[90:91], off offset:2048
	global_load_dwordx4 v[108:111], v[98:99], off
	global_load_dwordx4 v[112:115], v[98:99], off offset:2048
	s_mov_b64 exec, s[10:11]
	s_and_saveexec_b64 s[10:11], s[36:37]
	v_ashrrev_i32_e32 v7, 6, v20
	v_lshlrev_b32_e32 v12, 4, v7
	s_movk_i32 s13, 0x104
	v_mad_u32_u24 v13, v7, s13, v6
	v_add_co_u32_e32 v90, vcc, 0x2000, v90
	s_nop 1
	v_addc_co_u32_e32 v91, vcc, 0, v91, vcc
	v_add_co_u32_e32 v98, vcc, 0x2000, v98
	s_nop 1
	v_addc_co_u32_e32 v99, vcc, 0, v99, vcc
	s_waitcnt vmcnt(0)
	v_lshrrev_b64 v[8:9], v12, v[100:101]
	v_lshrrev_b64 v[10:11], v12, v[102:103]
	v_and_b32_e32 v8, 0xffff, v8
	v_lshl_or_b32 v100, v10, 16, v8
	ds_write_b32 v13, v100 offset:0
	v_lshrrev_b64 v[8:9], v12, v[104:105]
	v_lshrrev_b64 v[10:11], v12, v[106:107]
	v_and_b32_e32 v8, 0xffff, v8
	v_lshl_or_b32 v104, v10, 16, v8
	ds_write_b32 v13, v104 offset:2080
	v_lshrrev_b64 v[8:9], v12, v[108:109]
	v_lshrrev_b64 v[10:11], v12, v[110:111]
	v_and_b32_e32 v8, 0xffff, v8
	v_lshl_or_b32 v108, v10, 16, v8
	ds_write_b32 v13, v108 offset:4160
	v_lshrrev_b64 v[8:9], v12, v[112:113]
	v_lshrrev_b64 v[10:11], v12, v[114:115]
	v_and_b32_e32 v8, 0xffff, v8
	v_lshl_or_b32 v112, v10, 16, v8
	ds_write_b32 v13, v112 offset:6240
	global_load_dwordx4 v[100:103], v[90:91], off
	global_load_dwordx4 v[104:107], v[90:91], off offset:2048
	global_load_dwordx4 v[108:111], v[98:99], off
	global_load_dwordx4 v[112:115], v[98:99], off offset:2048
	s_waitcnt vmcnt(0)
	v_lshrrev_b64 v[8:9], v12, v[100:101]
	v_lshrrev_b64 v[10:11], v12, v[102:103]
	v_and_b32_e32 v8, 0xffff, v8
	v_lshl_or_b32 v100, v10, 16, v8
	ds_write_b32 v13, v100 offset:8320
	v_lshrrev_b64 v[8:9], v12, v[104:105]
	v_lshrrev_b64 v[10:11], v12, v[106:107]
	v_and_b32_e32 v8, 0xffff, v8
	v_lshl_or_b32 v104, v10, 16, v8
	ds_write_b32 v13, v104 offset:10400
	v_lshrrev_b64 v[8:9], v12, v[108:109]
	v_lshrrev_b64 v[10:11], v12, v[110:111]
	v_and_b32_e32 v8, 0xffff, v8
	v_lshl_or_b32 v108, v10, 16, v8
	ds_write_b32 v13, v108 offset:12480
	v_lshrrev_b64 v[8:9], v12, v[112:113]
	v_lshrrev_b64 v[10:11], v12, v[114:115]
	v_and_b32_e32 v8, 0xffff, v8
	v_lshl_or_b32 v112, v10, 16, v8
	ds_write_b32 v13, v112 offset:14560
	s_mov_b64 exec, s[10:11]
